# v33 + attention phase: static s_setprio 1 for waves 4-7 and packed v_pk_fma_f32 split into scalar fma pairs (timing-only)
# baseline (speedup 1.0000x reference)
.LBB0_845:
	s_cmp_lt_i32 s92, 9
	s_cselect_b64 s[2:3], -1, 0
	s_and_b64 s[0:1], s[2:3], s[0:1]
	v_writelane_b32 v254, s0, 6
	s_andn2_b64 vcc, exec, s[0:1]
	s_nop 0
	v_writelane_b32 v254, s1, 7
	v_writelane_b32 v254, s85, 8
	v_writelane_b32 v254, s76, 9
	s_nop 1
	v_writelane_b32 v254, s77, 10
	s_cbranch_vccnz .LBB0_1552
	s_cmp_lt_u32 s89, 4
	s_cbranch_scc1 .Lp8_prio_done
	s_setprio 1
.Lp8_prio_done:
	s_abs_i32 s33, s87
	v_cvt_f32_u32_e32 v0, s33
	s_sub_i32 s3, 0, s33
	s_add_i32 s0, s87, 0x1ff
	s_ashr_i32 s2, s0, 31
	v_rcp_iflag_f32_e32 v0, v0
	s_abs_i32 s0, s0
	s_ashr_i32 s40, s87, 31
	s_xor_b32 s2, s2, s40
	v_mul_f32_e32 v0, 0x4f7ffffe, v0
	v_cvt_u32_f32_e32 v0, v0
	s_mul_hi_i32 s1, s90, 0x92492493
	v_readfirstlane_b32 s41, v0
	s_mul_i32 s3, s3, s41
	s_mul_hi_u32 s3, s41, s3
	s_add_i32 s41, s41, s3
	s_mul_hi_u32 s3, s0, s41
	s_mul_i32 s4, s3, s33
	s_sub_i32 s0, s0, s4
	s_add_i32 s5, s3, 1
	s_sub_i32 s4, s0, s33
	s_cmp_ge_u32 s0, s33
	s_cselect_b32 s3, s5, s3
	s_cselect_b32 s0, s4, s0
	s_add_i32 s4, s3, 1
	s_cmp_ge_u32 s0, s33
	s_cselect_b32 s0, s4, s3
	s_xor_b32 s0, s0, s2
	s_sub_i32 s0, s0, s2
	s_mul_i32 s4, s0, s90
	s_add_i32 s0, s4, s0
	s_add_i32 s1, s1, s90
	s_min_i32 s42, s0, 0x200
	s_lshr_b32 s0, s1, 31
	s_ashr_i32 s1, s1, 8
	s_add_i32 s2, s1, s0
	s_mul_i32 s0, s2, 0x1c0
	s_sub_i32 s5, s90, s0
	s_cmpk_lt_i32 s5, 0xe0
	s_cselect_b64 s[0:1], -1, 0
	v_writelane_b32 v254, s0, 11
	s_add_u32 s57, s66, 0x6a00000
	s_addc_u32 s61, s67, 0
	v_writelane_b32 v254, s1, 12
	s_mul_i32 s1, s2, 0x1c00000
	s_mul_hi_i32 s0, s2, 0x1c00000
	s_add_u32 s6, s57, s1
	s_addc_u32 s7, s61, s0
	s_add_u32 s62, s66, 0x580000
	v_writelane_b32 v254, s6, 13
	s_addc_u32 s63, s67, 0
	s_mul_i32 s1, s2, 0xe000
	v_writelane_b32 v254, s7, 14
	s_mul_hi_i32 s0, s2, 0xe000
	s_add_u32 s6, s62, s1
	s_addc_u32 s7, s63, s0
	s_lshl_b32 s0, s89, 7
	s_add_i32 s0, s0, 0
	s_add_i32 s0, s0, 0x22a00
	s_add_u32 s68, s66, 0x380000
	v_writelane_b32 v254, s6, 15
	s_addc_u32 s69, s67, 0
	s_cmpk_lt_i32 s90, 0xe00
	v_writelane_b32 v254, s7, 16
	v_writelane_b32 v254, s0, 17
	s_cselect_b64 s[16:17], -1, 0
	s_add_u32 s0, s66, 0x22a00000
	s_addc_u32 s1, s67, 0
	v_writelane_b32 v254, s0, 18
	s_add_i32 s43, s87, 0xdff
	s_nop 0
	v_writelane_b32 v254, s1, 19
	s_bfe_u32 s0, s5, 0x5001a
	s_add_i32 s3, s5, s0
	s_sext_i32_i16 s0, s3
	s_lshr_b32 s0, s0, 5
	s_bfe_i64 s[0:1], s[0:1], 0x100000
	s_lshl_b64 s[0:1], s[0:1], 22
	v_writelane_b32 v254, s0, 20
	s_nop 1
	v_writelane_b32 v254, s1, 21
	s_and_b32 s0, s3, 0xffe0
	s_sub_i32 s0, s5, s0
	s_sext_i32_i16 s0, s0
	s_lshl_b32 s0, s0, 6
	v_writelane_b32 v254, s5, 22
	s_ashr_i32 s1, s0, 31
	v_writelane_b32 v254, s0, 23
	s_nop 1
	v_writelane_b32 v254, s1, 24
	s_lshl_b32 s0, s89, 3
	v_writelane_b32 v254, s0, 25
	v_writelane_b32 v254, s4, 26
	s_mul_hi_i32 s0, s2, 0x3800000
	v_writelane_b32 v254, s0, 27
	s_mul_i32 s0, s2, 0x3800000
	v_writelane_b32 v254, s0, 28
	s_mul_hi_i32 s1, s2, 0x1c00
	s_mul_i32 s0, s2, 0x1c00
	v_writelane_b32 v254, s0, 29
	s_cmp_gt_i32 s42, s4
	s_nop 0
	v_writelane_b32 v254, s1, 30
	s_mov_b64 s[0:1], -1
	s_cbranch_scc1 .LBB0_1025
	s_abs_i32 s1, s43
	s_mul_hi_u32 s2, s1, s41
	s_mul_i32 s3, s2, s33
	s_ashr_i32 s0, s43, 31
	s_sub_i32 s1, s1, s3
	s_xor_b32 s0, s0, s40
	s_add_i32 s3, s2, 1
	s_sub_i32 s4, s1, s33
	s_cmp_ge_u32 s1, s33
	s_cselect_b32 s2, s3, s2
	s_cselect_b32 s1, s4, s1
	s_add_i32 s3, s2, 1
	s_cmp_ge_u32 s1, s33
	s_cselect_b32 s1, s3, s2
	s_xor_b32 s1, s1, s0
	s_sub_i32 s44, s1, s0
	s_cmp_gt_i32 s44, 0
	s_cselect_b64 s[0:1], -1, 0
	s_and_b64 s[2:3], s[0:1], s[16:17]
	v_cndmask_b32_e64 v0, 0, 1, s[2:3]
	v_cmp_ne_u32_e64 s[0:1], 1, v0
	s_andn2_b64 vcc, exec, s[2:3]
	v_mbcnt_lo_u32_b32 v128, -1, 0
	v_mbcnt_hi_u32_b32 v128, -1, v128
	s_cbranch_vccnz .LBB0_850
	v_readlane_b32 s2, v254, 11
	v_readlane_b32 s3, v254, 12
	s_and_b64 vcc, exec, s[2:3]
	s_cbranch_vccz .LBB0_851
	s_add_i32 s2, 0, 0x23a90
	v_mov_b32_e32 v0, s2
	s_add_i32 s2, 0, 0x23a94
	s_waitcnt lgkmcnt(0)
	v_mov_b32_e32 v1, s2
	ds_read_b32 v0, v0
	ds_read_b32 v1, v1
	s_waitcnt lgkmcnt(0)
	v_readfirstlane_b32 s4, v0
	v_readfirstlane_b32 s5, v1
	s_mov_b32 s6, 0
	s_mov_b32 s46, 1
	s_cbranch_execz .LBB0_852
	s_branch .LBB0_853

.LBB0_1216:
	v_and_b32_e32 v51, 1, v193
	v_cmp_eq_u32_e32 vcc, 0, v51
	s_nop 5
	v_max_f32_e32 v51, v17, v17
	v_max_f32_e32 v52, v16, v16
	v_max_f32_e32 v51, v52, v51
	v_max3_f32 v51, v51, v18, v19
	v_max3_f32 v51, v51, v20, v21
	v_max3_f32 v51, v51, v22, v23
	v_max3_f32 v51, v51, v24, v25
	v_max3_f32 v51, v51, v26, v27
	v_max3_f32 v51, v51, v28, v29
	v_max3_f32 v51, v51, v30, v31
	v_max3_f32 v51, v51, v0, v1
	v_max3_f32 v51, v51, v2, v3
	v_max3_f32 v51, v51, v4, v5
	v_max3_f32 v51, v51, v6, v7
	v_max3_f32 v51, v51, v8, v9
	v_max3_f32 v51, v51, v10, v11
	v_max3_f32 v51, v51, v12, v13
	v_max3_f32 v51, v51, v14, v15
	v_mov_b32_e32 v52, v51
	s_cmp_lg_u32 s74, 0
	s_nop 0
	v_permlane32_swap_b32_e32 v51, v52
	s_cselect_b64 s[0:1], -1, 0
	v_max_f32_e32 v52, v52, v52
	v_max_f32_e32 v51, v51, v51
	s_lshl_b32 s76, s74, 2
	v_max_f32_e32 v51, v51, v52
	s_and_b64 vcc, s[0:1], vcc
	s_add_i32 s76, s76, 4
	v_lshlrev_b32_e32 v52, 3, v48
	v_and_b32_e32 v50, 0xc0, v50
	v_lshlrev_b32_e32 v53, 1, v48
	v_and_or_b32 v50, v52, 24, v50
	v_and_b32_e32 v53, 32, v53
	v_and_b32_e32 v52, 0x100, v52
	s_cmp_lg_u32 0, -1
	v_or3_b32 v50, v50, v53, v52
	s_cselect_b32 s0, 0, 0
	v_add_u32_e32 v187, s0, v50
	v_cndmask_b32_e32 v50, v51, v210, vcc
	v_add_f32_e32 v51, 0x7149f2ca, v50
	v_mul_f32_e32 v51, 0x3db504f3, v51
	v_max_f32_e32 v50, 0xf149f2ca, v50
	v_cmp_ge_f32_e64 s[0:1], s97, v51
	v_sub_f32_e32 v51, 0xf149f2ca, v50
	v_mul_f32_e32 v51, 0x3e0293ee, v51
	s_cmp_eq_u64 s[0:1], exec
	v_exp_f32_e32 v51, v51
	s_cselect_b64 s[0:1], -1, 0
	v_cndmask_b32_e64 v202, v50, v211, s[0:1]
	v_mul_f32_e32 v50, 0xbe0293ee, v202
	v_cndmask_b32_e32 v50, v50, v210, vcc
	v_cndmask_b32_e64 v201, v51, 1.0, s[0:1]
	v_mov_b32_e32 v51, v50
	v_fmamk_f32 v16, v16, 0x3e0293ee, v50
	v_fmamk_f32 v17, v17, 0x3e0293ee, v50
	v_fmamk_f32 v18, v18, 0x3e0293ee, v50
	v_fmamk_f32 v19, v19, 0x3e0293ee, v50
	v_fmamk_f32 v20, v20, 0x3e0293ee, v50
	v_fmamk_f32 v21, v21, 0x3e0293ee, v50
	v_fmamk_f32 v22, v22, 0x3e0293ee, v50
	v_fmamk_f32 v23, v23, 0x3e0293ee, v50
	v_fmamk_f32 v24, v24, 0x3e0293ee, v50
	v_fmamk_f32 v25, v25, 0x3e0293ee, v50
	v_fmamk_f32 v26, v26, 0x3e0293ee, v50
	v_fmamk_f32 v27, v27, 0x3e0293ee, v50
	v_fmamk_f32 v28, v28, 0x3e0293ee, v50
	v_fmamk_f32 v29, v29, 0x3e0293ee, v50
	v_fmamk_f32 v30, v30, 0x3e0293ee, v50
	v_fmac_f32_e32 v51, 0x3e0293ee, v31
	v_exp_f32_e32 v64, v16
	v_exp_f32_e32 v65, v17
	v_exp_f32_e32 v66, v18
	v_exp_f32_e32 v67, v19
	v_exp_f32_e32 v68, v20
	v_exp_f32_e32 v69, v21
	v_exp_f32_e32 v70, v22
	v_exp_f32_e32 v71, v23
	v_exp_f32_e32 v72, v24
	v_exp_f32_e32 v73, v25
	v_exp_f32_e32 v74, v26
	v_exp_f32_e32 v75, v27
	v_exp_f32_e32 v76, v28
	v_exp_f32_e32 v77, v29
	v_exp_f32_e32 v78, v30
	v_exp_f32_e32 v79, v51
	v_add_u32_e32 v190, 0, v49
	s_waitcnt vmcnt(0)
	s_waitcnt vmcnt(3)
	ds_write_b128 v199, v[36:39] offset:16384
	s_waitcnt vmcnt(1)
	ds_write_b128 v200, v[44:47] offset:16384
	ds_write_b128 v190, v[32:35] offset:49152
	s_waitcnt vmcnt(0)
	ds_write_b128 v190, v[40:43] offset:57344
	v_readlane_b32 s2, v254, 40
	v_mov_b32_e32 v32, v129
	v_mov_b32_e32 v33, v129
	v_mov_b32_e32 v46, v129
	v_mov_b32_e32 v47, v129
	v_fma_f32 v94, v14, s86, v50
	v_fma_f32 v95, v15, s86, v50
	v_fma_f32 v92, v12, s86, v50
	v_fma_f32 v93, v13, s86, v50
	v_fma_f32 v90, v10, s86, v50
	v_fma_f32 v91, v11, s86, v50
	v_fma_f32 v88, v8, s86, v50
	v_fma_f32 v89, v9, s86, v50
	v_fma_f32 v86, v6, s86, v50
	v_fma_f32 v87, v7, s86, v50
	v_fma_f32 v84, v4, s86, v50
	v_fma_f32 v85, v5, s86, v50
	v_fma_f32 v82, v2, s86, v50
	v_fma_f32 v83, v3, s86, v50
	v_fma_f32 v80, v0, s86, v50
	v_fma_f32 v81, v1, s86, v50
	v_cmp_gt_u32_e64 s[0:1], 32, v48
	v_lshl_add_u32 v188, v55, 2, s2
	s_add_u32 s82, s88, s62
	v_mov_b32_e32 v34, v129
	v_mov_b32_e32 v35, v129
	v_mov_b32_e32 v36, v129
	v_mov_b32_e32 v37, v129
	v_mov_b32_e32 v38, v129
	v_mov_b32_e32 v39, v129
	v_mov_b32_e32 v40, v129
	v_mov_b32_e32 v41, v129
	v_mov_b32_e32 v42, v129
	v_mov_b32_e32 v43, v129
	v_mov_b32_e32 v44, v129
	v_mov_b32_e32 v45, v129
	v_mov_b64_e32 v[62:63], v[46:47]
	v_mov_b64_e32 v[16:17], v[32:33]
	v_mov_b64_e32 v[0:1], v[32:33]
	v_mov_b32_e32 v181, v129
	s_mov_b32 s77, 3
	v_lshl_add_u32 v189, v184, 2, s2
	s_addc_u32 s83, s89, s63
	v_mov_b32_e32 v191, 0
	s_movk_i32 s78, 0x80
	v_mov_b64_e32 v[60:61], v[44:45]
	v_mov_b64_e32 v[58:59], v[42:43]
	v_mov_b64_e32 v[56:57], v[40:41]
	v_mov_b64_e32 v[54:55], v[38:39]
	v_mov_b64_e32 v[52:53], v[36:37]
	v_mov_b64_e32 v[50:51], v[34:35]
	v_mov_b64_e32 v[48:49], v[32:33]
	v_mov_b64_e32 v[18:19], v[34:35]
	v_mov_b64_e32 v[20:21], v[36:37]
	v_mov_b64_e32 v[22:23], v[38:39]
	v_mov_b64_e32 v[24:25], v[40:41]
	v_mov_b64_e32 v[26:27], v[42:43]
	v_mov_b64_e32 v[28:29], v[44:45]
	v_mov_b64_e32 v[30:31], v[46:47]
	v_mov_b64_e32 v[2:3], v[34:35]
	v_mov_b64_e32 v[4:5], v[36:37]
	v_mov_b64_e32 v[6:7], v[38:39]
	v_mov_b64_e32 v[8:9], v[40:41]
	v_mov_b64_e32 v[10:11], v[42:43]
	v_mov_b64_e32 v[12:13], v[44:45]
	v_mov_b64_e32 v[14:15], v[46:47]
	s_waitcnt lgkmcnt(0)
	s_barrier

.LBB0_1220:
	s_lshl_b32 s2, 1, s72
	v_and_b32_e32 v64, s2, v193
	v_cmp_eq_u32_e32 vcc, 0, v64
	ds_read_b64_tr_b16 v[64:65], v187 offset:0
	ds_read_b64_tr_b16 v[66:67], v187 offset:0x800
	ds_read_b64_tr_b16 v[68:69], v187 offset:0x1000
	ds_read_b64_tr_b16 v[70:71], v187 offset:0x1800
	ds_read_b64_tr_b16 v[72:73], v187 offset:0x2000
	ds_read_b64_tr_b16 v[74:75], v187 offset:0x2800
	ds_read_b64_tr_b16 v[76:77], v187 offset:0x3000
	ds_read_b64_tr_b16 v[78:79], v187 offset:0x3800
	s_waitcnt lgkmcnt(0)
	s_and_b64 vcc, s[68:69], vcc
	ds_read_b64_tr_b16 v[214:215], v187 offset:0x200
	ds_read_b64_tr_b16 v[216:217], v187 offset:0xa00
	ds_read_b64_tr_b16 v[218:219], v187 offset:0x1200
	ds_read_b64_tr_b16 v[220:221], v187 offset:0x1a00
	ds_read_b64_tr_b16 v[222:223], v187 offset:0x2200
	ds_read_b64_tr_b16 v[224:225], v187 offset:0x2a00
	ds_read_b64_tr_b16 v[226:227], v187 offset:0x3200
	ds_read_b64_tr_b16 v[228:229], v187 offset:0x3a00
	v_mfma_f32_32x32x16_bf16 v[32:47], v[80:83], v[64:67], v[32:47]
	v_max_f32_e32 v64, v113, v113
	v_max_f32_e32 v65, v112, v112
	v_max_f32_e32 v64, v65, v64
	v_max3_f32 v64, v64, v114, v115
	v_max3_f32 v64, v64, v116, v117
	v_max3_f32 v64, v64, v118, v119
	v_max3_f32 v64, v64, v120, v121
	v_mfma_f32_32x32x16_bf16 v[32:47], v[84:87], v[68:71], v[32:47]
	v_max3_f32 v64, v64, v122, v123
	v_max3_f32 v64, v64, v124, v125
	v_max3_f32 v64, v64, v126, v127
	v_max3_f32 v64, v64, v96, v97
	v_max3_f32 v64, v64, v98, v99
	v_max3_f32 v64, v64, v100, v101
	v_max3_f32 v64, v64, v102, v103
	v_mfma_f32_32x32x16_bf16 v[32:47], v[88:91], v[72:75], v[32:47]
	v_max3_f32 v64, v64, v104, v105
	v_max3_f32 v64, v64, v106, v107
	v_max3_f32 v64, v64, v108, v109
	v_max3_f32 v205, v64, v110, v111
	v_mfma_f32_32x32x16_bf16 v[32:47], v[92:95], v[76:79], v[32:47]
	s_waitcnt lgkmcnt(0)
	ds_read_b64_tr_b16 v[64:65], v187 offset:0x400
	ds_read_b64_tr_b16 v[66:67], v187 offset:0xc00
	ds_read_b64_tr_b16 v[68:69], v187 offset:0x1400
	ds_read_b64_tr_b16 v[70:71], v187 offset:0x1c00
	ds_read_b64_tr_b16 v[72:73], v187 offset:0x2400
	ds_read_b64_tr_b16 v[74:75], v187 offset:0x2c00
	ds_read_b64_tr_b16 v[76:77], v187 offset:0x3400
	ds_read_b64_tr_b16 v[78:79], v187 offset:0x3c00
	v_mfma_f32_32x32x16_bf16 v[48:63], v[80:83], v[214:217], v[48:63]
	v_mov_b32_e32 v206, v205
	s_nop 1
	v_permlane32_swap_b32_e32 v205, v206
	v_max_f32_e32 v206, v206, v206
	v_max_f32_e32 v205, v205, v205
	v_max_f32_e32 v205, v205, v206
	v_cndmask_b32_e32 v205, v205, v210, vcc
	v_mfma_f32_32x32x16_bf16 v[48:63], v[84:87], v[218:221], v[48:63]
	v_max_f32_e32 v207, v202, v202
	v_sub_f32_e32 v206, v205, v202
	v_max_f32_e32 v205, v207, v205
	v_mul_f32_e32 v206, 0x3db504f3, v206
	v_sub_f32_e32 v207, v202, v205
	v_cmp_ge_f32_e64 s[2:3], s97, v206
	v_mul_f32_e32 v206, 0x3e0293ee, v207
	v_mfma_f32_32x32x16_bf16 v[48:63], v[88:91], v[222:225], v[48:63]
	v_exp_f32_e32 v207, v206
	s_cmp_eq_u64 s[2:3], exec
	s_cselect_b64 s[2:3], -1, 0
	v_cndmask_b32_e64 v206, v205, v202, s[2:3]
	v_cndmask_b32_e64 v205, v207, 1.0, s[2:3]
	v_mul_f32_e32 v202, 0xbe0293ee, v206
	v_cndmask_b32_e32 v202, v202, v210, vcc
	v_mfma_f32_32x32x16_bf16 v[48:63], v[92:95], v[226:229], v[48:63]
	s_waitcnt lgkmcnt(0)
	ds_read_b64_tr_b16 v[214:215], v187 offset:0x600
	ds_read_b64_tr_b16 v[216:217], v187 offset:0xe00
	ds_read_b64_tr_b16 v[218:219], v187 offset:0x1600
	ds_read_b64_tr_b16 v[220:221], v187 offset:0x1e00
	ds_read_b64_tr_b16 v[222:223], v187 offset:0x2600
	ds_read_b64_tr_b16 v[224:225], v187 offset:0x2e00
	ds_read_b64_tr_b16 v[226:227], v187 offset:0x3600
	ds_read_b64_tr_b16 v[228:229], v187 offset:0x3e00
	v_mfma_f32_32x32x16_bf16 v[16:31], v[80:83], v[64:67], v[16:31]
	v_fma_f32 v66, v114, s86, v202
	v_fma_f32 v67, v115, s86, v202
	v_fma_f32 v64, v112, s86, v202
	v_fma_f32 v65, v113, s86, v202
	v_fma_f32 v110, v110, s86, v202
	v_fma_f32 v111, v111, s86, v202
	v_fma_f32 v108, v108, s86, v202
	v_fma_f32 v109, v109, s86, v202
	v_fma_f32 v106, v106, s86, v202
	v_fma_f32 v107, v107, s86, v202
	v_fma_f32 v104, v104, s86, v202
	v_fma_f32 v105, v105, s86, v202
	v_fma_f32 v102, v102, s86, v202
	v_fma_f32 v103, v103, s86, v202
	v_mfma_f32_32x32x16_bf16 v[16:31], v[84:87], v[68:71], v[16:31]
	v_fma_f32 v70, v118, s86, v202
	v_fma_f32 v71, v119, s86, v202
	v_fma_f32 v68, v116, s86, v202
	v_fma_f32 v69, v117, s86, v202
	v_fma_f32 v100, v100, s86, v202
	v_fma_f32 v101, v101, s86, v202
	v_fma_f32 v98, v98, s86, v202
	v_fma_f32 v99, v99, s86, v202
	v_fma_f32 v96, v96, s86, v202
	v_fma_f32 v97, v97, s86, v202
	v_mfma_f32_32x32x16_bf16 v[16:31], v[88:91], v[72:75], v[16:31]
	v_fma_f32 v74, v122, s86, v202
	v_fma_f32 v75, v123, s86, v202
	v_fma_f32 v72, v120, s86, v202
	v_fma_f32 v73, v121, s86, v202
	v_mfma_f32_32x32x16_bf16 v[16:31], v[92:95], v[76:79], v[16:31]
	v_fma_f32 v78, v126, s86, v202
	v_fma_f32 v79, v127, s86, v202
	v_fma_f32 v76, v124, s86, v202
	v_fma_f32 v77, v125, s86, v202
	s_waitcnt lgkmcnt(0)
	v_mfma_f32_32x32x16_bf16 v[0:15], v[80:83], v[214:217], v[0:15]
	v_exp_f32_e32 v112, v64
	v_exp_f32_e32 v113, v65
	v_exp_f32_e32 v114, v66
	v_exp_f32_e32 v115, v67
	v_exp_f32_e32 v116, v68
	v_exp_f32_e32 v117, v69
	v_exp_f32_e32 v118, v70
	v_mfma_f32_32x32x16_bf16 v[0:15], v[84:87], v[218:221], v[0:15]
	v_exp_f32_e32 v119, v71
	v_exp_f32_e32 v120, v72
	v_exp_f32_e32 v121, v73
	v_exp_f32_e32 v122, v74
	v_exp_f32_e32 v123, v75
	v_exp_f32_e32 v124, v76
	v_exp_f32_e32 v125, v77
	v_mfma_f32_32x32x16_bf16 v[0:15], v[88:91], v[222:225], v[0:15]
	v_exp_f32_e32 v126, v78
	v_exp_f32_e32 v127, v79
	s_barrier
	s_waitcnt vmcnt(0)
	v_mfma_f32_32x32x16_bf16 v[0:15], v[92:95], v[226:229], v[0:15]
	v_cmp_gt_f32_e32 vcc, 1.0, v205
	s_waitcnt vmcnt(3)
	ds_write_b128 v199, v[130:133]
	s_waitcnt vmcnt(2)
	ds_write_b128 v200, v[134:137]
	s_waitcnt vmcnt(1)
	ds_write_b128 v190, v[168:171] offset:32768
	s_waitcnt vmcnt(0)
	ds_write_b128 v190, v[176:179] offset:40960
	s_cbranch_vccz .LBB0_1224
	s_and_saveexec_b64 s[2:3], s[0:1]
	ds_write_b32 v189, v205 offset:128
	s_or_b64 exec, exec, s[2:3]
	s_waitcnt lgkmcnt(0)
	ds_read_b128 v[64:67], v188 offset:224
	ds_read_b128 v[68:71], v188 offset:192
	ds_read_b128 v[72:75], v188 offset:160
	ds_read_b128 v[76:79], v188 offset:128
	s_waitcnt lgkmcnt(3)
	v_pk_mul_f32 v[46:47], v[46:47], v[66:67]
	s_waitcnt lgkmcnt(2)
	v_pk_mul_f32 v[42:43], v[42:43], v[70:71]
	s_waitcnt lgkmcnt(1)
	v_pk_mul_f32 v[38:39], v[38:39], v[74:75]
	s_waitcnt lgkmcnt(0)
	v_pk_mul_f32 v[34:35], v[34:35], v[78:79]
	v_pk_mul_f32 v[44:45], v[44:45], v[64:65]
	v_pk_mul_f32 v[40:41], v[40:41], v[68:69]
	v_pk_mul_f32 v[36:37], v[36:37], v[72:73]
	v_pk_mul_f32 v[32:33], v[32:33], v[76:77]
	v_pk_mul_f32 v[62:63], v[62:63], v[66:67]
	v_pk_mul_f32 v[58:59], v[58:59], v[70:71]
	v_pk_mul_f32 v[54:55], v[54:55], v[74:75]
	v_pk_mul_f32 v[50:51], v[50:51], v[78:79]
	v_pk_mul_f32 v[60:61], v[60:61], v[64:65]
	v_pk_mul_f32 v[56:57], v[56:57], v[68:69]
	v_pk_mul_f32 v[52:53], v[52:53], v[72:73]
	v_pk_mul_f32 v[48:49], v[48:49], v[76:77]
	v_pk_mul_f32 v[30:31], v[30:31], v[66:67]
	v_pk_mul_f32 v[26:27], v[26:27], v[70:71]
	v_pk_mul_f32 v[22:23], v[22:23], v[74:75]
	v_pk_mul_f32 v[18:19], v[18:19], v[78:79]
	v_pk_mul_f32 v[28:29], v[28:29], v[64:65]
	v_pk_mul_f32 v[24:25], v[24:25], v[68:69]
	v_pk_mul_f32 v[20:21], v[20:21], v[72:73]
	v_pk_mul_f32 v[16:17], v[16:17], v[76:77]
	v_pk_mul_f32 v[14:15], v[14:15], v[66:67]
	v_pk_mul_f32 v[10:11], v[10:11], v[70:71]
	v_pk_mul_f32 v[6:7], v[6:7], v[74:75]
	v_pk_mul_f32 v[2:3], v[2:3], v[78:79]
	v_pk_mul_f32 v[12:13], v[12:13], v[64:65]
	v_pk_mul_f32 v[8:9], v[8:9], v[68:69]
	v_pk_mul_f32 v[4:5], v[4:5], v[72:73]
	v_pk_mul_f32 v[0:1], v[0:1], v[76:77]

.LBB0_1229:
	s_lshl_b32 s2, 1, s90
	v_and_b32_e32 v96, s2, v193
	v_cmp_eq_u32_e32 vcc, 0, v96
	ds_read_b64_tr_b16 v[96:97], v187 offset:0x4000
	ds_read_b64_tr_b16 v[98:99], v187 offset:0x4800
	ds_read_b64_tr_b16 v[100:101], v187 offset:0x5000
	ds_read_b64_tr_b16 v[102:103], v187 offset:0x5800
	ds_read_b64_tr_b16 v[104:105], v187 offset:0x6000
	ds_read_b64_tr_b16 v[106:107], v187 offset:0x6800
	ds_read_b64_tr_b16 v[108:109], v187 offset:0x7000
	ds_read_b64_tr_b16 v[110:111], v187 offset:0x7800
	s_waitcnt lgkmcnt(0)
	s_and_b64 vcc, s[72:73], vcc
	ds_read_b64_tr_b16 v[214:215], v187 offset:0x4200
	ds_read_b64_tr_b16 v[216:217], v187 offset:0x4a00
	ds_read_b64_tr_b16 v[218:219], v187 offset:0x5200
	ds_read_b64_tr_b16 v[220:221], v187 offset:0x5a00
	ds_read_b64_tr_b16 v[222:223], v187 offset:0x6200
	ds_read_b64_tr_b16 v[224:225], v187 offset:0x6a00
	ds_read_b64_tr_b16 v[226:227], v187 offset:0x7200
	ds_read_b64_tr_b16 v[228:229], v187 offset:0x7a00
	v_mfma_f32_32x32x16_bf16 v[32:47], v[112:115], v[96:99], v[32:47]
	v_max_f32_e32 v96, v81, v81
	v_max_f32_e32 v97, v80, v80
	v_max_f32_e32 v96, v97, v96
	v_max3_f32 v96, v96, v82, v83
	v_max3_f32 v96, v96, v84, v85
	v_max3_f32 v96, v96, v86, v87
	v_max3_f32 v96, v96, v88, v89
	v_mfma_f32_32x32x16_bf16 v[32:47], v[116:119], v[100:103], v[32:47]
	v_max3_f32 v96, v96, v90, v91
	v_max3_f32 v96, v96, v92, v93
	v_max3_f32 v96, v96, v94, v95
	v_max3_f32 v96, v96, v64, v65
	v_max3_f32 v96, v96, v66, v67
	v_max3_f32 v96, v96, v68, v69
	v_max3_f32 v96, v96, v70, v71
	v_mfma_f32_32x32x16_bf16 v[32:47], v[120:123], v[104:107], v[32:47]
	v_max3_f32 v96, v96, v72, v73
	v_max3_f32 v96, v96, v74, v75
	v_max3_f32 v96, v96, v76, v77
	v_max3_f32 v182, v96, v78, v79
	v_mfma_f32_32x32x16_bf16 v[32:47], v[124:127], v[108:111], v[32:47]
	s_waitcnt lgkmcnt(0)
	ds_read_b64_tr_b16 v[96:97], v187 offset:0x4400
	ds_read_b64_tr_b16 v[98:99], v187 offset:0x4c00
	ds_read_b64_tr_b16 v[100:101], v187 offset:0x5400
	ds_read_b64_tr_b16 v[102:103], v187 offset:0x5c00
	ds_read_b64_tr_b16 v[104:105], v187 offset:0x6400
	ds_read_b64_tr_b16 v[106:107], v187 offset:0x6c00
	ds_read_b64_tr_b16 v[108:109], v187 offset:0x7400
	ds_read_b64_tr_b16 v[110:111], v187 offset:0x7c00
	v_mfma_f32_32x32x16_bf16 v[48:63], v[112:115], v[214:217], v[48:63]
	v_mov_b32_e32 v183, v182
	s_nop 1
	v_permlane32_swap_b32_e32 v182, v183
	v_max_f32_e32 v183, v183, v183
	v_max_f32_e32 v182, v182, v182
	v_max_f32_e32 v182, v182, v183
	v_cndmask_b32_e32 v182, v182, v210, vcc
	v_mfma_f32_32x32x16_bf16 v[48:63], v[116:119], v[218:221], v[48:63]
	v_sub_f32_e32 v183, v182, v206
	v_mul_f32_e32 v183, 0x3db504f3, v183
	v_cmp_ge_f32_e64 s[2:3], s97, v183
	s_cmp_eq_u64 s[2:3], exec
	v_max_f32_e32 v183, v206, v206
	v_max_f32_e32 v182, v183, v182
	s_cselect_b64 s[2:3], -1, 0
	v_mfma_f32_32x32x16_bf16 v[48:63], v[120:123], v[222:225], v[48:63]
	v_cndmask_b32_e64 v202, v182, v206, s[2:3]
	v_mul_f32_e32 v183, 0xbe0293ee, v202
	v_cndmask_b32_e32 v230, v183, v210, vcc
	v_mfma_f32_32x32x16_bf16 v[48:63], v[124:127], v[226:229], v[48:63]
	s_waitcnt lgkmcnt(0)
	ds_read_b64_tr_b16 v[214:215], v187 offset:0x4600
	ds_read_b64_tr_b16 v[216:217], v187 offset:0x4e00
	ds_read_b64_tr_b16 v[218:219], v187 offset:0x5600
	ds_read_b64_tr_b16 v[220:221], v187 offset:0x5e00
	ds_read_b64_tr_b16 v[222:223], v187 offset:0x6600
	ds_read_b64_tr_b16 v[224:225], v187 offset:0x6e00
	ds_read_b64_tr_b16 v[226:227], v187 offset:0x7600
	ds_read_b64_tr_b16 v[228:229], v187 offset:0x7e00
	v_mfma_f32_32x32x16_bf16 v[16:31], v[112:115], v[96:99], v[16:31]
	v_fma_f32 v98, v82, s86, v230
	v_fma_f32 v99, v83, s86, v230
	v_fma_f32 v96, v80, s86, v230
	v_fma_f32 v97, v81, s86, v230
	v_fma_f32 v82, v66, s86, v230
	v_fma_f32 v83, v67, s86, v230
	v_fma_f32 v80, v64, s86, v230
	v_fma_f32 v81, v65, s86, v230
	v_mfma_f32_32x32x16_bf16 v[16:31], v[116:119], v[100:103], v[16:31]
	v_fma_f32 v102, v86, s86, v230
	v_fma_f32 v103, v87, s86, v230
	v_fma_f32 v100, v84, s86, v230
	v_fma_f32 v101, v85, s86, v230
	v_fma_f32 v86, v70, s86, v230
	v_fma_f32 v87, v71, s86, v230
	v_fma_f32 v84, v68, s86, v230
	v_fma_f32 v85, v69, s86, v230
	v_mfma_f32_32x32x16_bf16 v[16:31], v[120:123], v[104:107], v[16:31]
	v_fma_f32 v106, v90, s86, v230
	v_fma_f32 v107, v91, s86, v230
	v_fma_f32 v104, v88, s86, v230
	v_fma_f32 v105, v89, s86, v230
	v_fma_f32 v90, v74, s86, v230
	v_fma_f32 v91, v75, s86, v230
	v_fma_f32 v88, v72, s86, v230
	v_fma_f32 v89, v73, s86, v230
	v_mfma_f32_32x32x16_bf16 v[16:31], v[124:127], v[108:111], v[16:31]
	v_fma_f32 v110, v94, s86, v230
	v_fma_f32 v111, v95, s86, v230
	v_fma_f32 v108, v92, s86, v230
	v_fma_f32 v109, v93, s86, v230
	v_fma_f32 v94, v78, s86, v230
	v_fma_f32 v95, v79, s86, v230
	v_fma_f32 v92, v76, s86, v230
	v_fma_f32 v93, v77, s86, v230
	s_nop 0
	s_waitcnt lgkmcnt(0)
	v_mfma_f32_32x32x16_bf16 v[0:15], v[112:115], v[214:217], v[0:15]
	v_exp_f32_e32 v64, v96
	v_exp_f32_e32 v65, v97
	v_exp_f32_e32 v66, v98
	v_exp_f32_e32 v67, v99
	v_exp_f32_e32 v68, v100
	v_exp_f32_e32 v69, v101
	v_exp_f32_e32 v70, v102
	v_mfma_f32_32x32x16_bf16 v[0:15], v[116:119], v[218:221], v[0:15]
	v_exp_f32_e32 v71, v103
	v_exp_f32_e32 v72, v104
	v_exp_f32_e32 v73, v105
	v_exp_f32_e32 v74, v106
	v_exp_f32_e32 v75, v107
	v_exp_f32_e32 v76, v108
	v_exp_f32_e32 v77, v109
	v_mfma_f32_32x32x16_bf16 v[0:15], v[120:123], v[222:225], v[0:15]
	v_exp_f32_e32 v78, v110
	v_exp_f32_e32 v79, v111
	s_andn2_b64 vcc, exec, s[68:69]
	s_barrier
	v_mfma_f32_32x32x16_bf16 v[0:15], v[124:127], v[226:229], v[0:15]
	s_cbranch_vccnz .LBB0_1231
	s_waitcnt vmcnt(0)
	s_waitcnt vmcnt(3)
	ds_write_b128 v199, v[130:133] offset:16384
	s_waitcnt vmcnt(2)
	ds_write_b128 v200, v[134:137] offset:16384
	s_waitcnt vmcnt(1)
	ds_write_b128 v190, v[168:171] offset:49152
	s_waitcnt vmcnt(0)
	ds_write_b128 v190, v[176:179] offset:57344

.LBB0_1552:
	s_setprio 0
	s_cmp_gt_i32 s93, 9
	v_readlane_b32 s2, v254, 6
	s_cselect_b64 s[0:1], -1, 0
	v_readlane_b32 s3, v254, 7
	s_and_b64 s[2:3], s[2:3], s[0:1]
	s_andn2_b64 vcc, exec, s[2:3]
	s_cbranch_vccnz .LBB0_1608
	s_waitcnt vmcnt(0)
	s_cmp_gt_u32 s94, 63
	s_waitcnt vmcnt(0) lgkmcnt(0)
	s_barrier
	s_cbranch_scc1 .LBB0_1607
	v_mbcnt_lo_u32_b32 v0, -1, 0
	v_mbcnt_hi_u32_b32 v0, -1, v0
	s_nop 0
	v_cmp_eq_u32_e32 vcc, 0, v0
	s_and_saveexec_b64 s[2:3], vcc
	s_cbranch_execz .LBB0_1606
	s_add_i32 s4, 0, 0x23960
	v_mov_b32_e32 v0, s4
	s_waitcnt vmcnt(0) expcnt(0) lgkmcnt(0)
	ds_read_b32 v2, v0
	s_add_i32 s4, 0, 0x23964
	v_mov_b32_e32 v0, s4
	ds_read_b32 v0, v0
	s_waitcnt lgkmcnt(1)
	v_cmp_ne_u32_e32 vcc, 0, v2
	s_cbranch_vccnz .LBB0_1570
	v_readlane_b32 s4, v254, 0
	v_readlane_b32 s5, v254, 1
	s_load_dwordx2 s[8:9], s[4:5], 0x4
	s_add_u32 s4, s66, 0x4200
	s_addc_u32 s5, s67, 0
	s_add_u32 s6, s66, 0x4400
	s_addc_u32 s7, s67, 0
	s_waitcnt lgkmcnt(0)
	s_mul_i32 s33, s8, s87
	s_add_u32 s8, s66, 0x4500
	s_mul_i32 s33, s33, s9
	s_addc_u32 s9, s67, 0
	s_add_u32 s10, s66, 0x4600
	s_addc_u32 s11, s67, 0
	s_add_u32 s12, s66, 0x4700
	s_addc_u32 s13, s67, 0
	s_add_u32 s14, s66, 0x4800
	s_addc_u32 s15, s67, 0
	s_add_u32 s16, s66, 0x4900
	s_addc_u32 s17, s67, 0
	s_add_u32 s18, s66, 0x4a00
	s_addc_u32 s19, s67, 0
	s_add_u32 s20, s66, 0x4b00
	s_addc_u32 s21, s67, 0
	s_add_u32 s22, s66, 0x4c00
	s_addc_u32 s23, s67, 0
	s_add_u32 s24, s66, 0x4d00
	s_addc_u32 s25, s67, 0
	s_add_u32 s26, s66, 0x4e00
	s_addc_u32 s27, s67, 0
	s_add_u32 s28, s66, 0x4f00
	s_addc_u32 s29, s67, 0
	s_add_u32 s30, s66, 0x5000
	s_addc_u32 s31, s67, 0
	s_add_u32 s34, s66, 0x5100
	s_addc_u32 s35, s67, 0
	s_add_u32 s36, s66, 0x5200
	s_addc_u32 s37, s67, 0
	s_add_u32 s38, s66, 0x5300
	s_addc_u32 s39, s67, 0
	s_mov_b32 s46, 1
	v_mov_b32_e32 v16, 0
	s_branch .LBB0_1558
